# GEMM streams: the trailing half-workgroup decodes the next unit in front of its barrier (end of its MFMA block), overlapping the leading half's decode behind that barrier
# baseline (speedup 1.0000x reference)
.LBB0_259:
	ds_read_b128 v[20:23], v210
	ds_read_b128 v[24:27], v210 offset:1024
	ds_read_b128 v[28:31], v210 offset:2048
	ds_read_b128 v[32:35], v210 offset:3072
	ds_read_b128 v[4:7], v211
	ds_read_b128 v[8:11], v211 offset:1024
	ds_read_b128 v[12:15], v211 offset:2048
	ds_read_b128 v[16:19], v211 offset:3072
	s_add_u32 s2, s6, s12
	s_addc_u32 s3, s7, s13
	v_add_u32_e32 v192, 0xc000, v191
	s_add_u32 s2, s2, 0x80
	v_mov_b32_e32 v2, v182
	v_readfirstlane_b32 s26, v192
	v_add_u32_e32 v192, 0xe000, v191
	ds_read_b128 v[218:221], v214
	ds_read_b128 v[222:225], v214 offset:1024
	ds_read_b128 v[226:229], v215
	ds_read_b128 v[230:233], v215 offset:1024
	ds_read_b128 v[234:237], v216
	ds_read_b128 v[238:241], v216 offset:1024
	ds_read_b128 v[242:245], v217
	ds_read_b128 v[246:249], v217 offset:1024
	s_addc_u32 s3, s3, 0
	s_mov_b32 m0, s26
	v_readfirstlane_b32 s26, v192
	global_load_lds_dwordx4 v2, s[2:3]
	v_mov_b32_e32 v2, v183
	s_mov_b32 m0, s26
	s_nop 0
	global_load_lds_dwordx4 v2, s[2:3]
	s_waitcnt vmcnt(8)
	s_waitcnt lgkmcnt(0)
	s_barrier
	s_setprio 1
	s_waitcnt lgkmcnt(0)
	v_mfma_scale_f32_16x16x128_f8f6f4 v[176:179], v[20:27], v[218:225], v[176:179], v186, v185 op_sel_hi:[0,0,0]
	v_mfma_scale_f32_16x16x128_f8f6f4 v[172:175], v[28:35], v[218:225], v[172:175], v186, v185 op_sel_hi:[0,0,0]
	v_mfma_scale_f32_16x16x128_f8f6f4 v[168:171], v[20:27], v[226:233], v[168:171], v186, v185 op_sel_hi:[0,0,0]
	v_mfma_scale_f32_16x16x128_f8f6f4 v[164:167], v[28:35], v[226:233], v[164:167], v186, v185 op_sel_hi:[0,0,0]
	v_mfma_scale_f32_16x16x128_f8f6f4 v[160:163], v[20:27], v[234:241], v[160:163], v186, v185 op_sel_hi:[0,0,0]
	v_mfma_scale_f32_16x16x128_f8f6f4 v[156:159], v[28:35], v[234:241], v[156:159], v186, v185 op_sel_hi:[0,0,0]
	v_mfma_scale_f32_16x16x128_f8f6f4 v[152:155], v[20:27], v[242:249], v[152:155], v186, v185 op_sel_hi:[0,0,0]
	v_mfma_scale_f32_16x16x128_f8f6f4 v[148:151], v[28:35], v[242:249], v[148:151], v186, v185 op_sel_hi:[0,0,0]
	s_setprio 0
	s_setprio 1
	v_mfma_scale_f32_16x16x128_f8f6f4 v[112:115], v[4:11], v[218:225], v[112:115], v186, v185 op_sel_hi:[0,0,0]
	v_mfma_scale_f32_16x16x128_f8f6f4 v[108:111], v[12:19], v[218:225], v[108:111], v186, v185 op_sel_hi:[0,0,0]
	v_mfma_scale_f32_16x16x128_f8f6f4 v[104:107], v[4:11], v[226:233], v[104:107], v186, v185 op_sel_hi:[0,0,0]
	v_mfma_scale_f32_16x16x128_f8f6f4 v[100:103], v[12:19], v[226:233], v[100:103], v186, v185 op_sel_hi:[0,0,0]
	v_mfma_scale_f32_16x16x128_f8f6f4 v[96:99], v[4:11], v[234:241], v[96:99], v186, v185 op_sel_hi:[0,0,0]
	v_mfma_scale_f32_16x16x128_f8f6f4 v[92:95], v[12:19], v[234:241], v[92:95], v186, v185 op_sel_hi:[0,0,0]
	v_mfma_scale_f32_16x16x128_f8f6f4 v[88:91], v[4:11], v[242:249], v[88:91], v186, v185 op_sel_hi:[0,0,0]
	v_mfma_scale_f32_16x16x128_f8f6f4 v[84:87], v[12:19], v[242:249], v[84:87], v186, v185 op_sel_hi:[0,0,0]
	s_cmp_lg_u32 s25, 4
	s_cbranch_scc1 .Lnx0_done
	s_cmp_eq_u64 s[38:39], 0
	s_cbranch_scc0 .Lnx0_done
	s_cmpk_gt_u32 s15, 0xd7f
	s_mov_b64 s[20:21], 0
	s_cbranch_scc1 .Lnx0_done
	v_readlane_b32 s2, v255, 41
	v_readlane_b32 s4, v255, 40
	v_mov_b32_e32 v2, v0
	s_mov_b64 s[20:21], -1
	v_ashrrev_i32_e32 v181, 31, v2
	v_lshrrev_b32_e32 v181, 26, v181
	v_lshlrev_b32_e32 v180, 4, v2
	v_add_u32_e32 v181, v2, v181
	v_bfe_i32 v2, v2, 27, 1
	s_waitcnt lgkmcnt(0)
	s_lshr_b32 s2, s2, 16
	v_lshrrev_b32_e32 v2, 22, v2
	s_cmp_lg_u32 s2, 0
	v_add_u32_e32 v2, v180, v2
	s_cselect_b64 s[2:3], -1, 0
	v_and_b32_e32 v2, 0xfffffc00, v2
	s_cmp_lg_u64 s[2:3], 0
	v_sub_u32_e32 v2, v180, v2
	s_addc_u32 s16, s4, s15
	s_lshr_b32 s3, s15, 3
	v_lshrrev_b32_e32 v180, 4, v2
	s_and_b32 s2, s15, 7
	s_add_i32 s4, s3, 0xffffff28
	v_bitop3_b32 v2, v180, v2, 32 bitop3:0x6c
	s_cmpk_lt_u32 s15, 0x6c0
	v_ashrrev_i32_e32 v182, 31, v2
	s_cselect_b32 s3, s3, s4
	s_cmpk_gt_u32 s15, 0x6bf
	v_lshrrev_b32_e32 v182, 26, v182
	s_cselect_b32 s4, 8, 0
	s_and_b32 s5, s3, 7
	v_add_u32_e32 v182, v2, v182
	s_or_b32 s4, s5, s4
	v_lshrrev_b32_e32 v183, 6, v182
	v_and_b32_e32 v182, 0xc0, v182
	s_lshr_b32 s82, s3, 3
	s_lshl_b32 s3, s4, 3
	v_ashrrev_i32_e32 v181, 6, v181
	v_sub_u32_e32 v2, v2, v182
	s_or_b32 s14, s3, s2
	v_lshlrev_b32_e32 v180, 3, v181
	v_lshlrev_b32_e32 v181, 5, v181
	v_ashrrev_i16_sdwa v2, v196, sext(v2) dst_sel:DWORD dst_unused:UNUSED_PAD src0_sel:DWORD src1_sel:BYTE_0
	s_lshl_b64 s[2:3], s[82:83], 18
	v_and_b32_e32 v180, 0x3ffff0, v180
	v_and_b32_e32 v181, 32, v181
	v_bfe_i32 v2, v2, 0, 16
	s_add_u32 s4, s19, s2
	s_addc_u32 s5, s22, s3
	s_lshl_b32 s2, s14, 18
	v_add_lshl_u32 v180, v183, v180, 10
	v_add_lshl_u32 v2, v181, v2, 1
	v_add3_u32 v180, v180, s2, v2
	v_add_u32_e32 v181, 0x10000, v180
	v_add_u32_e32 v182, 0x20000, v180
	v_add_u32_e32 v183, 0x30000, v180
	s_mov_b64 s[6:7], s[8:9]
	s_mov_b32 s15, s16
	s_mov_b32 s16, s82
.Lnx0_done:
	s_cmp_lg_u32 s25, 4
	s_setprio 0
	s_barrier
	s_cbranch_scc1 .LBB0_262
	s_cmp_eq_u64 s[38:39], 0
	s_cbranch_scc1 .LBB0_257
	s_cmpk_gt_u32 s15, 0xd7f
	s_mov_b64 s[20:21], 0
	s_cbranch_scc1 .LBB0_257
	v_readlane_b32 s2, v255, 41
	v_readlane_b32 s4, v255, 40
	v_mov_b32_e32 v2, v0
	s_mov_b64 s[20:21], -1
	v_ashrrev_i32_e32 v181, 31, v2
	v_lshrrev_b32_e32 v181, 26, v181
	v_lshlrev_b32_e32 v180, 4, v2
	v_add_u32_e32 v181, v2, v181
	v_bfe_i32 v2, v2, 27, 1
	s_waitcnt lgkmcnt(0)
	s_lshr_b32 s2, s2, 16
	v_lshrrev_b32_e32 v2, 22, v2
	s_cmp_lg_u32 s2, 0
	v_add_u32_e32 v2, v180, v2
	s_cselect_b64 s[2:3], -1, 0
	v_and_b32_e32 v2, 0xfffffc00, v2
	s_cmp_lg_u64 s[2:3], 0
	v_sub_u32_e32 v2, v180, v2
	s_addc_u32 s16, s4, s15
	s_lshr_b32 s3, s15, 3
	v_lshrrev_b32_e32 v180, 4, v2
	s_and_b32 s2, s15, 7
	s_add_i32 s4, s3, 0xffffff28
	v_bitop3_b32 v2, v180, v2, 32 bitop3:0x6c
	s_cmpk_lt_u32 s15, 0x6c0
	v_ashrrev_i32_e32 v182, 31, v2
	s_cselect_b32 s3, s3, s4
	s_cmpk_gt_u32 s15, 0x6bf
	v_lshrrev_b32_e32 v182, 26, v182
	s_cselect_b32 s4, 8, 0
	s_and_b32 s5, s3, 7
	v_add_u32_e32 v182, v2, v182
	s_or_b32 s4, s5, s4
	v_lshrrev_b32_e32 v183, 6, v182
	v_and_b32_e32 v182, 0xc0, v182
	s_lshr_b32 s82, s3, 3
	s_lshl_b32 s3, s4, 3
	v_ashrrev_i32_e32 v181, 6, v181
	v_sub_u32_e32 v2, v2, v182
	s_or_b32 s14, s3, s2
	v_lshlrev_b32_e32 v180, 3, v181
	v_lshlrev_b32_e32 v181, 5, v181
	v_ashrrev_i16_sdwa v2, v196, sext(v2) dst_sel:DWORD dst_unused:UNUSED_PAD src0_sel:DWORD src1_sel:BYTE_0
	s_lshl_b64 s[2:3], s[82:83], 18
	v_and_b32_e32 v180, 0x3ffff0, v180
	v_and_b32_e32 v181, 32, v181
	v_bfe_i32 v2, v2, 0, 16
	s_add_u32 s4, s19, s2
	s_addc_u32 s5, s22, s3
	s_lshl_b32 s2, s14, 18
	v_add_lshl_u32 v180, v183, v180, 10
	v_add_lshl_u32 v2, v181, v2, 1
	v_add3_u32 v180, v180, s2, v2
	v_add_u32_e32 v181, 0x10000, v180
	v_add_u32_e32 v182, 0x20000, v180
	v_add_u32_e32 v183, 0x30000, v180
	s_mov_b64 s[6:7], s[8:9]
	s_mov_b32 s15, s16
	s_mov_b32 s16, s82
	s_branch .LBB0_257

.LBB0_1248:
	ds_read_b128 v[20:23], v212
	ds_read_b128 v[24:27], v212 offset:1024
	ds_read_b128 v[28:31], v212 offset:2048
	ds_read_b128 v[32:35], v212 offset:3072
	ds_read_b128 v[4:7], v213
	ds_read_b128 v[8:11], v213 offset:1024
	ds_read_b128 v[12:15], v213 offset:2048
	ds_read_b128 v[16:19], v213 offset:3072
	s_lshl_b32 s2, s30, 7
	s_add_u32 s2, s6, s2
	s_addc_u32 s3, s7, 0
	v_add_u32_e32 v181, 0xc000, v202
	s_add_u32 s2, s2, 0x80
	v_mov_b32_e32 v2, v185
	v_readfirstlane_b32 s31, v181
	v_add_u32_e32 v181, 0xe000, v202
	ds_read_b128 v[220:223], v216
	ds_read_b128 v[224:227], v216 offset:1024
	ds_read_b128 v[228:231], v217
	ds_read_b128 v[232:235], v217 offset:1024
	ds_read_b128 v[236:239], v218
	ds_read_b128 v[240:243], v218 offset:1024
	ds_read_b128 v[244:247], v219
	ds_read_b128 v[248:251], v219 offset:1024
	s_addc_u32 s3, s3, 0
	s_mov_b32 m0, s31
	v_readfirstlane_b32 s31, v181
	global_load_lds_dwordx4 v2, s[2:3]
	v_mov_b32_e32 v2, v186
	s_mov_b32 m0, s31
	s_nop 0
	global_load_lds_dwordx4 v2, s[2:3]
	s_waitcnt vmcnt(8)
	s_waitcnt lgkmcnt(0)
	s_barrier
	s_setprio 1
	s_waitcnt lgkmcnt(0)
	v_mfma_scale_f32_16x16x128_f8f6f4 v[176:179], v[20:27], v[220:227], v[176:179], v188, v187 op_sel_hi:[0,0,0]
	v_mfma_scale_f32_16x16x128_f8f6f4 v[168:171], v[28:35], v[220:227], v[168:171], v188, v187 op_sel_hi:[0,0,0]
	v_mfma_scale_f32_16x16x128_f8f6f4 v[160:163], v[20:27], v[228:235], v[160:163], v188, v187 op_sel_hi:[0,0,0]
	v_mfma_scale_f32_16x16x128_f8f6f4 v[152:155], v[28:35], v[228:235], v[152:155], v188, v187 op_sel_hi:[0,0,0]
	v_mfma_scale_f32_16x16x128_f8f6f4 v[144:147], v[20:27], v[236:243], v[144:147], v188, v187 op_sel_hi:[0,0,0]
	v_mfma_scale_f32_16x16x128_f8f6f4 v[136:139], v[28:35], v[236:243], v[136:139], v188, v187 op_sel_hi:[0,0,0]
	v_mfma_scale_f32_16x16x128_f8f6f4 v[128:131], v[20:27], v[244:251], v[128:131], v188, v187 op_sel_hi:[0,0,0]
	v_mfma_scale_f32_16x16x128_f8f6f4 v[120:123], v[28:35], v[244:251], v[120:123], v188, v187 op_sel_hi:[0,0,0]
	s_setprio 0
	s_setprio 1
	s_add_i32 s31, s30, 2
	v_mfma_scale_f32_16x16x128_f8f6f4 v[172:175], v[4:11], v[220:227], v[172:175], v188, v187 op_sel_hi:[0,0,0]
	v_mfma_scale_f32_16x16x128_f8f6f4 v[164:167], v[12:19], v[220:227], v[164:167], v188, v187 op_sel_hi:[0,0,0]
	v_mfma_scale_f32_16x16x128_f8f6f4 v[156:159], v[4:11], v[228:235], v[156:159], v188, v187 op_sel_hi:[0,0,0]
	v_mfma_scale_f32_16x16x128_f8f6f4 v[148:151], v[12:19], v[228:235], v[148:151], v188, v187 op_sel_hi:[0,0,0]
	v_mfma_scale_f32_16x16x128_f8f6f4 v[140:143], v[4:11], v[236:243], v[140:143], v188, v187 op_sel_hi:[0,0,0]
	v_mfma_scale_f32_16x16x128_f8f6f4 v[132:135], v[12:19], v[236:243], v[132:135], v188, v187 op_sel_hi:[0,0,0]
	v_mfma_scale_f32_16x16x128_f8f6f4 v[124:127], v[4:11], v[244:251], v[124:127], v188, v187 op_sel_hi:[0,0,0]
	v_mfma_scale_f32_16x16x128_f8f6f4 v[116:119], v[12:19], v[244:251], v[116:119], v188, v187 op_sel_hi:[0,0,0]
	s_cmp_lg_u32 s30, 6
	s_cbranch_scc1 .Lnx1_done
	s_cmp_eq_u64 s[38:39], 0
	s_cbranch_scc0 .Lnx1_done
	s_mov_b64 s[2:3], -1
	s_cmp_ge_u32 s18, s16
	s_mov_b64 s[12:13], -1
	s_cbranch_scc1 .Lnx1_1

.Lnx1_1:
	s_andn2_b64 vcc, exec, s[12:13]
	s_cbranch_vccz .Lnx1_2
	s_mov_b32 s18, s33
	s_mov_b64 s[2:3], -1
	s_cmp_ge_u32 s18, s16
	s_mov_b64 s[12:13], -1
	s_cbranch_scc1 .Lnx1_1
	s_branch .Lnx1_0
.Lnx1_2:
	s_mov_b32 s82, 0
	s_andn2_b64 vcc, exec, s[2:3]
	s_mov_b64 s[12:13], 0
	s_cbranch_vccz .Lnx1_done
	s_lshl_b32 s2, s35, 3
	s_or_b32 s24, s2, s34
	s_mov_b32 s4, s29
	s_mov_b32 s5, s28
	s_mov_b32 s3, s27
	v_and_b32_e32 v2, 63, v0
	v_lshlrev_b32_e32 v2, 2, v2
	v_add_u32_e32 v2, 0x21004, v2
	ds_read_b32 v2, v2
	s_waitcnt lgkmcnt(0)
	v_cmp_ge_i32_e64 s[84:85], s24, v2
	s_bcnt1_i32_b32 s17, s84
	s_lshl_b32 s2, s17, 2
	s_add_i32 s2, s2, 0x21000
	v_mov_b32_e32 v2, v0
	s_add_i32 s2, s17, s14
	v_ashrrev_i32_e32 v182, 31, v2
	v_lshrrev_b32_e32 v182, 26, v182
	v_lshlrev_b32_e32 v181, 4, v2
	v_add_u32_e32 v182, v2, v182
	v_bfe_i32 v2, v2, 27, 1
	v_lshrrev_b32_e32 v2, 22, v2
	v_add_u32_e32 v2, v181, v2
	v_and_b32_e32 v2, 0xfffffc00, v2
	s_bfe_u32 s25, s18, 0x30006
	v_sub_u32_e32 v2, v181, v2
	s_ashr_i32 s3, s2, 31
	v_lshrrev_b32_e32 v181, 4, v2
	s_lshl_b32 s4, s25, 18
	s_lshl_b64 s[2:3], s[2:3], 21
	v_bitop3_b32 v2, v181, v2, 32 bitop3:0x6c
	s_add_u32 s2, s22, s2
	v_ashrrev_i32_e32 v181, 31, v2
	s_addc_u32 s3, s23, s3
	v_lshrrev_b32_e32 v181, 26, v181
	s_add_u32 s4, s2, s4
	v_ashrrev_i32_e32 v182, 6, v182
	v_add_u32_e32 v181, v2, v181
	s_addc_u32 s5, s3, 0
	s_lshl_b32 s2, s19, 10
	v_ashrrev_i32_e32 v183, 6, v181
	v_lshlrev_b32_e32 v182, 5, v182
	v_and_b32_e32 v181, 0xc0, v181
	s_add_i32 s2, s2, 0
	v_and_b32_e32 v185, 32, v182
	v_sub_u32_e32 v2, v2, v181
	v_and_b32_e32 v181, 0xffffffc0, v182
	s_add_i32 s2, s2, 0x22000
	v_lshlrev_b32_e32 v182, 2, v183
	v_add3_u32 v181, s2, v181, v182
	ds_read2st64_b32 v[182:183], v181 offset1:1
	ds_read2st64_b32 v[192:193], v181 offset0:2 offset1:3
	v_ashrrev_i16_sdwa v2, v196, sext(v2) dst_sel:DWORD dst_unused:UNUSED_PAD src0_sel:DWORD src1_sel:BYTE_0
	v_bfe_i32 v2, v2, 0, 16
	v_add_lshl_u32 v2, v185, v2, 1
	s_waitcnt lgkmcnt(0)
	v_lshl_add_u32 v182, v182, 10, v2
	v_lshl_add_u32 v183, v183, 10, v2
	v_lshl_add_u32 v185, v192, 10, v2
	v_lshl_add_u32 v186, v193, 10, v2
	s_add_i32 s19, s19, 1
	s_mov_b64 s[12:13], -1
	s_mov_b64 s[6:7], s[8:9]
	s_mov_b32 s18, s33
.Lnx1_done:
	s_cmp_lg_u32 s30, 6
	s_setprio 0
	s_barrier
	s_cbranch_scc1 .LBB0_1253
	s_cmp_eq_u64 s[38:39], 0
	s_cbranch_scc1 .LBB0_1259
	s_mov_b64 s[2:3], -1
	s_cmp_ge_u32 s18, s16
	s_mov_b64 s[12:13], -1
	s_cbranch_scc1 .LBB0_1251

.LBB0_1387:
	ds_read_b128 v[20:23], v212
	ds_read_b128 v[24:27], v212 offset:1024
	ds_read_b128 v[28:31], v212 offset:2048
	ds_read_b128 v[32:35], v212 offset:3072
	ds_read_b128 v[4:7], v213
	ds_read_b128 v[8:11], v213 offset:1024
	ds_read_b128 v[12:15], v213 offset:2048
	ds_read_b128 v[16:19], v213 offset:3072
	s_lshl_b32 s2, s23, 7
	s_add_u32 s2, s4, s2
	s_addc_u32 s3, s5, 0
	v_add_u32_e32 v181, 0xc000, v202
	s_add_u32 s2, s2, 0x80
	v_mov_b32_e32 v2, v184
	v_readfirstlane_b32 s24, v181
	v_add_u32_e32 v181, 0xe000, v202
	ds_read_b128 v[222:225], v216
	ds_read_b128 v[226:229], v216 offset:1024
	ds_read_b128 v[230:233], v217
	ds_read_b128 v[234:237], v217 offset:1024
	ds_read_b128 v[238:241], v218
	ds_read_b128 v[242:245], v218 offset:1024
	ds_read_b128 v[36:39], v219
	ds_read_b128 v[40:43], v219 offset:1024
	s_addc_u32 s3, s3, 0
	s_mov_b32 m0, s24
	v_readfirstlane_b32 s24, v181
	global_load_lds_dwordx4 v2, s[2:3]
	v_mov_b32_e32 v2, v185
	s_mov_b32 m0, s24
	s_nop 0
	global_load_lds_dwordx4 v2, s[2:3]
	s_waitcnt vmcnt(8)
	s_waitcnt lgkmcnt(0)
	s_barrier
	s_setprio 1
	s_waitcnt lgkmcnt(0)
	v_mfma_scale_f32_16x16x128_f8f6f4 v[176:179], v[20:27], v[222:229], v[176:179], v188, v187 op_sel_hi:[0,0,0]
	v_mfma_scale_f32_16x16x128_f8f6f4 v[172:175], v[28:35], v[222:229], v[172:175], v188, v187 op_sel_hi:[0,0,0]
	v_mfma_scale_f32_16x16x128_f8f6f4 v[168:171], v[20:27], v[230:237], v[168:171], v188, v187 op_sel_hi:[0,0,0]
	v_mfma_scale_f32_16x16x128_f8f6f4 v[164:167], v[28:35], v[230:237], v[164:167], v188, v187 op_sel_hi:[0,0,0]
	v_mfma_scale_f32_16x16x128_f8f6f4 v[160:163], v[20:27], v[238:245], v[160:163], v188, v187 op_sel_hi:[0,0,0]
	v_mfma_scale_f32_16x16x128_f8f6f4 v[156:159], v[28:35], v[238:245], v[156:159], v188, v187 op_sel_hi:[0,0,0]
	v_mfma_scale_f32_16x16x128_f8f6f4 v[152:155], v[20:27], v[36:43], v[152:155], v188, v187 op_sel_hi:[0,0,0]
	v_mfma_scale_f32_16x16x128_f8f6f4 v[148:151], v[28:35], v[36:43], v[148:151], v188, v187 op_sel_hi:[0,0,0]
	s_setprio 0
	s_setprio 1
	s_add_i32 s24, s23, 2
	v_mfma_scale_f32_16x16x128_f8f6f4 v[120:123], v[4:11], v[222:229], v[120:123], v188, v187 op_sel_hi:[0,0,0]
	v_mfma_scale_f32_16x16x128_f8f6f4 v[116:119], v[12:19], v[222:229], v[116:119], v188, v187 op_sel_hi:[0,0,0]
	v_mfma_scale_f32_16x16x128_f8f6f4 v[112:115], v[4:11], v[230:237], v[112:115], v188, v187 op_sel_hi:[0,0,0]
	v_mfma_scale_f32_16x16x128_f8f6f4 v[108:111], v[12:19], v[230:237], v[108:111], v188, v187 op_sel_hi:[0,0,0]
	v_mfma_scale_f32_16x16x128_f8f6f4 v[96:99], v[4:11], v[238:245], v[96:99], v188, v187 op_sel_hi:[0,0,0]
	v_mfma_scale_f32_16x16x128_f8f6f4 v[92:95], v[12:19], v[238:245], v[92:95], v188, v187 op_sel_hi:[0,0,0]
	v_mfma_scale_f32_16x16x128_f8f6f4 v[88:91], v[4:11], v[36:43], v[88:91], v188, v187 op_sel_hi:[0,0,0]
	v_mfma_scale_f32_16x16x128_f8f6f4 v[84:87], v[12:19], v[36:43], v[84:87], v188, v187 op_sel_hi:[0,0,0]
	s_cmp_lg_u32 s23, 6
	s_cbranch_scc1 .Lnx2_done
	s_cmp_eq_u64 s[38:39], 0
	s_cbranch_scc0 .Lnx2_done
	s_mov_b64 s[2:3], -1
	s_cmp_ge_u32 s14, s13
	s_mov_b64 s[10:11], -1
	s_cbranch_scc1 .Lnx2_1

.Lnx2_1:
	s_andn2_b64 vcc, exec, s[10:11]
	s_cbranch_vccz .Lnx2_2
	s_mov_b32 s14, s25
	s_mov_b64 s[2:3], -1
	s_cmp_ge_u32 s14, s13
	s_mov_b64 s[10:11], -1
	s_cbranch_scc1 .Lnx2_1
	s_branch .Lnx2_0
.Lnx2_2:
	s_mov_b32 s82, 0
	s_andn2_b64 vcc, exec, s[2:3]
	s_mov_b64 s[10:11], 0
	s_cbranch_vccz .Lnx2_done
	s_lshl_b32 s2, s27, 3
	s_or_b32 s18, s2, s26
	s_mov_b32 s4, s22
	s_mov_b32 s5, s21
	s_mov_b32 s3, s20
	v_and_b32_e32 v2, 63, v0
	v_lshlrev_b32_e32 v2, 2, v2
	v_add_u32_e32 v2, 0x21004, v2
	ds_read_b32 v2, v2
	s_waitcnt lgkmcnt(0)
	v_cmp_ge_i32_e64 s[84:85], s18, v2
	s_bcnt1_i32_b32 s15, s84
	s_lshl_b32 s2, s15, 2
	s_add_i32 s2, s2, 0x21000
	v_mov_b32_e32 v2, v0
	s_load_dwordx2 s[2:3], s[0:1], 0xd0
	v_ashrrev_i32_e32 v37, 31, v2
	v_lshrrev_b32_e32 v37, 26, v37
	v_lshlrev_b32_e32 v36, 4, v2
	v_add_u32_e32 v37, v2, v37
	v_bfe_i32 v2, v2, 27, 1
	v_lshrrev_b32_e32 v2, 22, v2
	v_add_u32_e32 v2, v36, v2
	v_and_b32_e32 v2, 0xfffffc00, v2
	s_bfe_u32 s19, s14, 0x20006
	s_add_i32 s16, s16, 1
	v_sub_u32_e32 v2, v36, v2
	v_lshrrev_b32_e32 v36, 4, v2
	s_waitcnt lgkmcnt(0)
	s_add_u32 s4, s2, 0x52182000
	v_bitop3_b32 v2, v36, v2, 32 bitop3:0x6c
	s_addc_u32 s5, s3, 0
	s_add_i32 s6, s15, s17
	v_ashrrev_i32_e32 v38, 31, v2
	s_ashr_i32 s7, s6, 31
	v_lshrrev_b32_e32 v38, 26, v38
	s_lshl_b32 s10, s19, 18
	s_lshl_b64 s[6:7], s[6:7], 20
	v_add_u32_e32 v38, v2, v38
	s_add_u32 s2, s2, s6
	v_lshrrev_b32_e32 v39, 6, v38
	v_and_b32_e32 v38, 0xc0, v38
	s_addc_u32 s3, s3, s7
	v_ashrrev_i32_e32 v37, 6, v37
	v_sub_u32_e32 v2, v2, v38
	s_add_u32 s2, s2, s10
	v_lshlrev_b32_e32 v36, 3, v37
	v_lshlrev_b32_e32 v37, 5, v37
	v_ashrrev_i16_sdwa v2, v196, sext(v2) dst_sel:DWORD dst_unused:UNUSED_PAD src0_sel:DWORD src1_sel:BYTE_0
	s_addc_u32 s3, s3, 0
	v_and_b32_e32 v36, 0x3ffff0, v36
	v_and_b32_e32 v37, 32, v37
	v_bfe_i32 v2, v2, 0, 16
	s_add_u32 s6, s2, 0x126a2000
	s_addc_u32 s7, s3, 0
	s_lshl_b32 s2, s18, 18
	v_add_lshl_u32 v36, v39, v36, 10
	v_add_lshl_u32 v2, v37, v2, 1
	v_add3_u32 v182, v36, s2, v2
	v_add_u32_e32 v183, 0x10000, v182
	v_add_u32_e32 v184, 0x20000, v182
	v_add_u32_e32 v185, 0x30000, v182
	s_mov_b64 s[10:11], -1
	s_mov_b32 s14, s25
.Lnx2_done:
	s_cmp_lg_u32 s23, 6
	s_setprio 0
	s_barrier
	s_cbranch_scc1 .LBB0_1392
	s_cmp_eq_u64 s[38:39], 0
	s_cbranch_scc1 .LBB0_1398
	s_mov_b64 s[2:3], -1
	s_cmp_ge_u32 s14, s13
	s_mov_b64 s[10:11], -1
	s_cbranch_scc1 .LBB0_1390
